# stack: no dangling converter prefetch + P6 table reuse + batched converter copy-out + batched SGU bias loads
# baseline (speedup 1.0000x reference)
; #define G_SCHED __builtin_amdgcn_sched_barrier(0)
; #define CI_LOAD(R, kt) do { _Pragma("unroll") for (int _j = 0; _j < 16; ++_j) R[_j] = __builtin_nontemporal_load((const f32x4*)(src + (size_t)((kt) * 128 + _j) * LDB)); } while (0)
; template <int LDB>
; __device__ __forceinline__ void convert_image(const float* __restrict__ W, int col0, int col1, unsigned char* __restrict__ img, LAS3 char* lds, int wid) {
;     ...
;     f32x4 ra[16], rb[16];
;     CI_LOAD(ra, 0);
;     for (int kt = 0; kt < 16; kt += 2) {
;         CI_LOAD(rb, kt + 1); G_SCHED;
;         CI_CONV(ra, kt); G_SCHED;
;         CI_LOAD(ra, (kt + 2 < 16) ? kt + 2 : 15); G_SCHED;
.Lcw_gu:
	s_waitcnt vmcnt(34)
	v_cvt_scalef32_pk_fp8_f32 v152, v0, v4, s22
	s_waitcnt vmcnt(30)
	v_cvt_scalef32_pk_fp8_f32 v153, v16, v20, s22
	s_waitcnt vmcnt(26)
	v_cvt_scalef32_pk_fp8_f32 v154, v32, v36, s22
	s_waitcnt vmcnt(22)
	v_cvt_scalef32_pk_fp8_f32 v155, v48, v52, s22
	v_cvt_scalef32_pk_fp8_f32 v152, v8, v12, s22 op_sel:[0,0,0,1]
	v_cvt_scalef32_pk_fp8_f32 v153, v24, v28, s22 op_sel:[0,0,0,1]
	v_cvt_scalef32_pk_fp8_f32 v154, v40, v44, s22 op_sel:[0,0,0,1]
	s_waitcnt vmcnt(20)
	v_cvt_scalef32_pk_fp8_f32 v155, v56, v60, s22 op_sel:[0,0,0,1]
	ds_write_b128 v141, v[152:155]
	v_mov_b32_e32 v152, v123
	v_mov_b32_e32 v153, v123
	v_mov_b32_e32 v154, v123
	v_mov_b32_e32 v155, v123
	v_cvt_scalef32_pk_fp8_f32 v152, v1, v5, s22
	v_cvt_scalef32_pk_fp8_f32 v153, v17, v21, s22
	v_cvt_scalef32_pk_fp8_f32 v154, v33, v37, s22
	v_cvt_scalef32_pk_fp8_f32 v155, v49, v53, s22
	v_cvt_scalef32_pk_fp8_f32 v152, v9, v13, s22 op_sel:[0,0,0,1]
	v_cvt_scalef32_pk_fp8_f32 v153, v25, v29, s22 op_sel:[0,0,0,1]
	v_cvt_scalef32_pk_fp8_f32 v154, v41, v45, s22 op_sel:[0,0,0,1]
	v_cvt_scalef32_pk_fp8_f32 v155, v57, v61, s22 op_sel:[0,0,0,1]
	ds_write_b128 v141, v[152:155] offset:128
	v_mov_b32_e32 v152, v123
	v_mov_b32_e32 v0, v123
	v_cvt_scalef32_pk_fp8_f32 v152, v2, v6, s22
	v_mov_b32_e32 v153, v123
	v_mov_b32_e32 v154, v123
	v_mov_b32_e32 v155, v123
	v_cvt_scalef32_pk_fp8_f32 v0, v3, v7, s22
	v_mov_b32_e32 v1, v123
	v_mov_b32_e32 v2, v123
	v_mov_b32_e32 v3, v123
	v_cvt_scalef32_pk_fp8_f32 v153, v18, v22, s22
	v_cvt_scalef32_pk_fp8_f32 v154, v34, v38, s22
	v_cvt_scalef32_pk_fp8_f32 v155, v50, v54, s22
	v_cvt_scalef32_pk_fp8_f32 v1, v19, v23, s22
	v_cvt_scalef32_pk_fp8_f32 v2, v35, v39, s22
	v_cvt_scalef32_pk_fp8_f32 v3, v51, v55, s22
	v_cvt_scalef32_pk_fp8_f32 v152, v10, v14, s22 op_sel:[0,0,0,1]
	v_cvt_scalef32_pk_fp8_f32 v153, v26, v30, s22 op_sel:[0,0,0,1]
	v_cvt_scalef32_pk_fp8_f32 v154, v42, v46, s22 op_sel:[0,0,0,1]
	v_cvt_scalef32_pk_fp8_f32 v155, v58, v62, s22 op_sel:[0,0,0,1]
	v_cvt_scalef32_pk_fp8_f32 v0, v11, v15, s22 op_sel:[0,0,0,1]
	v_cvt_scalef32_pk_fp8_f32 v1, v27, v31, s22 op_sel:[0,0,0,1]
	v_cvt_scalef32_pk_fp8_f32 v2, v43, v47, s22 op_sel:[0,0,0,1]
	v_cvt_scalef32_pk_fp8_f32 v3, v59, v63, s22 op_sel:[0,0,0,1]
	ds_write_b128 v142, v[152:155]
	ds_write_b128 v143, v[0:3]
	s_waitcnt lgkmcnt(0)
	s_barrier
	ds_read_b128 v[0:3], v144
	ds_read_b128 v[4:7], v144 offset:1024
	ds_read_b128 v[8:11], v144 offset:2048
	ds_read_b128 v[12:15], v144 offset:3072
	s_nop 3
	s_waitcnt lgkmcnt(3)
	global_store_dwordx4 v137, v[0:3], s[0:1] sc1
	s_waitcnt lgkmcnt(2)
	global_store_dwordx4 v138, v[4:7], s[0:1] sc1
	s_waitcnt lgkmcnt(1)
	global_store_dwordx4 v139, v[8:11], s[0:1] sc1
	s_waitcnt lgkmcnt(0)
	global_store_dwordx4 v140, v[12:15], s[0:1] sc1
	s_nop 1
	s_cmp_eq_u32 s13, 14
	s_cbranch_scc1 .Lnp_gu
	s_min_u32 s4, s13, 13
	s_lshl_b32 s4, s4, 21
	v_lshl_add_u64 v[56:57], v[132:133], 0, s[4:5]
	s_mov_b32 s4, 0x400000
	v_add_co_u32_e32 v0, vcc, s4, v56
	s_mov_b32 s4, 0x404000
	s_nop 0
	v_addc_co_u32_e32 v1, vcc, 0, v57, vcc
	v_add_co_u32_e32 v4, vcc, s4, v56
	s_mov_b32 s4, 0x408000
	s_nop 0
	v_addc_co_u32_e32 v5, vcc, 0, v57, vcc
	v_add_co_u32_e32 v8, vcc, s4, v56
	s_mov_b32 s4, 0x40c000
	s_nop 0
	v_addc_co_u32_e32 v9, vcc, 0, v57, vcc
	v_add_co_u32_e32 v12, vcc, s4, v56
	s_mov_b32 s4, 0x410000
	s_nop 0
	v_addc_co_u32_e32 v13, vcc, 0, v57, vcc
	v_add_co_u32_e32 v16, vcc, s4, v56
	s_mov_b32 s4, 0x414000
	s_nop 0
	v_addc_co_u32_e32 v17, vcc, 0, v57, vcc
	v_add_co_u32_e32 v20, vcc, s4, v56
	s_mov_b32 s4, 0x418000
	s_nop 0
	v_addc_co_u32_e32 v21, vcc, 0, v57, vcc
	v_add_co_u32_e32 v24, vcc, s4, v56
	s_mov_b32 s4, 0x41c000
	s_nop 0
	v_addc_co_u32_e32 v25, vcc, 0, v57, vcc
	v_add_co_u32_e32 v28, vcc, s4, v56
	s_mov_b32 s4, 0x420000
	s_nop 0
	v_addc_co_u32_e32 v29, vcc, 0, v57, vcc
	v_add_co_u32_e32 v32, vcc, s4, v56
	s_mov_b32 s4, 0x424000
	s_nop 0
	v_addc_co_u32_e32 v33, vcc, 0, v57, vcc
	v_add_co_u32_e32 v36, vcc, s4, v56
	s_mov_b32 s4, 0x428000
	s_nop 0
	v_addc_co_u32_e32 v37, vcc, 0, v57, vcc
	v_add_co_u32_e32 v40, vcc, s4, v56
	s_mov_b32 s4, 0x42c000
	s_nop 0
	v_addc_co_u32_e32 v41, vcc, 0, v57, vcc
	v_add_co_u32_e32 v44, vcc, s4, v56
	s_mov_b32 s4, 0x430000
	s_nop 0
	v_addc_co_u32_e32 v45, vcc, 0, v57, vcc
	v_add_co_u32_e32 v48, vcc, s4, v56
	s_mov_b32 s4, 0x434000
	s_nop 0
	v_addc_co_u32_e32 v49, vcc, 0, v57, vcc
	v_add_co_u32_e32 v52, vcc, s4, v56
	s_mov_b32 s4, 0x438000
	s_nop 0
	v_addc_co_u32_e32 v53, vcc, 0, v57, vcc
	v_add_co_u32_e32 v58, vcc, s4, v56
	s_mov_b32 s4, 0x43c000
	s_nop 0
	v_addc_co_u32_e32 v59, vcc, 0, v57, vcc
	v_add_co_u32_e32 v60, vcc, s4, v56
	global_load_dwordx4 v[0:3], v[0:1], off nt
	s_nop 0
	global_load_dwordx4 v[4:7], v[4:5], off nt
	v_addc_co_u32_e32 v61, vcc, 0, v57, vcc
	global_load_dwordx4 v[8:11], v[8:9], off nt
	s_nop 0
	global_load_dwordx4 v[12:15], v[12:13], off nt
	s_nop 0
	global_load_dwordx4 v[16:19], v[16:17], off nt
	s_nop 0
	global_load_dwordx4 v[20:23], v[20:21], off nt
	s_nop 0
	global_load_dwordx4 v[24:27], v[24:25], off nt
	s_nop 0
	global_load_dwordx4 v[28:31], v[28:29], off nt
	s_nop 0
	global_load_dwordx4 v[32:35], v[32:33], off nt
	s_nop 0
	global_load_dwordx4 v[36:39], v[36:37], off nt
	s_nop 0
	global_load_dwordx4 v[40:43], v[40:41], off nt
	s_nop 0
	global_load_dwordx4 v[44:47], v[44:45], off nt
	s_nop 0
	global_load_dwordx4 v[48:51], v[48:49], off nt
	s_nop 0
	global_load_dwordx4 v[52:55], v[52:53], off nt
	s_nop 0
	global_load_dwordx4 v[56:59], v[58:59], off nt
	s_nop 0
	global_load_dwordx4 v[60:63], v[60:61], off nt

; #define G_SCHED __builtin_amdgcn_sched_barrier(0)
; #define CI_LOAD(R, kt) do { _Pragma("unroll") for (int _j = 0; _j < 16; ++_j) R[_j] = __builtin_nontemporal_load((const f32x4*)(src + (size_t)((kt) * 128 + _j) * LDB)); } while (0)
; template <int LDB>
; __device__ __forceinline__ void convert_image(const float* __restrict__ W, int col0, int col1, unsigned char* __restrict__ img, LAS3 char* lds, int wid) {
;     ...
;     f32x4 ra[16], rb[16];
;     CI_LOAD(ra, 0);
;     for (int kt = 0; kt < 16; kt += 2) {
;         CI_LOAD(rb, kt + 1); G_SCHED;
;         CI_CONV(ra, kt); G_SCHED;
;         CI_LOAD(ra, (kt + 2 < 16) ? kt + 2 : 15); G_SCHED;
;         CI_CONV(rb, kt + 1); G_SCHED;
;     }
.Lnw2_gu:
	s_waitcnt vmcnt(20)
	v_cvt_scalef32_pk_fp8_f32 v155, v116, v124, s22 op_sel:[0,0,0,1]
	ds_write_b128 v141, v[152:155] offset:32768
	v_mov_b32_e32 v152, v123
	v_mov_b32_e32 v153, v123
	v_mov_b32_e32 v154, v123
	v_mov_b32_e32 v155, v123
	v_cvt_scalef32_pk_fp8_f32 v152, v129, v65, s22
	v_cvt_scalef32_pk_fp8_f32 v153, v77, v81, s22
	v_cvt_scalef32_pk_fp8_f32 v154, v93, v97, s22
	v_cvt_scalef32_pk_fp8_f32 v155, v109, v113, s22
	v_cvt_scalef32_pk_fp8_f32 v152, v69, v73, s22 op_sel:[0,0,0,1]
	v_cvt_scalef32_pk_fp8_f32 v153, v85, v89, s22 op_sel:[0,0,0,1]
	v_cvt_scalef32_pk_fp8_f32 v154, v101, v105, s22 op_sel:[0,0,0,1]
	v_cvt_scalef32_pk_fp8_f32 v155, v117, v125, s22 op_sel:[0,0,0,1]
	ds_write_b128 v141, v[152:155] offset:32896
	v_mov_b32_e32 v152, v123
	v_mov_b32_e32 v153, v123
	v_mov_b32_e32 v154, v123
	v_mov_b32_e32 v155, v123
	v_mov_b32_e32 v120, v123
	v_mov_b32_e32 v121, v123
	v_mov_b32_e32 v122, v123
	v_cvt_scalef32_pk_fp8_f32 v152, v130, v66, s22
	v_cvt_scalef32_pk_fp8_f32 v153, v78, v82, s22
	v_cvt_scalef32_pk_fp8_f32 v154, v94, v98, s22
	v_cvt_scalef32_pk_fp8_f32 v155, v110, v114, s22
	v_cvt_scalef32_pk_fp8_f32 v120, v131, v67, s22
	v_cvt_scalef32_pk_fp8_f32 v121, v79, v83, s22
	v_cvt_scalef32_pk_fp8_f32 v122, v95, v99, s22
	v_cvt_scalef32_pk_fp8_f32 v123, v111, v115, s22
	v_cvt_scalef32_pk_fp8_f32 v152, v70, v74, s22 op_sel:[0,0,0,1]
	v_cvt_scalef32_pk_fp8_f32 v153, v86, v90, s22 op_sel:[0,0,0,1]
	v_cvt_scalef32_pk_fp8_f32 v154, v102, v106, s22 op_sel:[0,0,0,1]
	v_cvt_scalef32_pk_fp8_f32 v155, v118, v126, s22 op_sel:[0,0,0,1]
	v_cvt_scalef32_pk_fp8_f32 v120, v71, v75, s22 op_sel:[0,0,0,1]
	v_cvt_scalef32_pk_fp8_f32 v121, v87, v91, s22 op_sel:[0,0,0,1]
	v_cvt_scalef32_pk_fp8_f32 v122, v103, v107, s22 op_sel:[0,0,0,1]
	v_cvt_scalef32_pk_fp8_f32 v123, v119, v127, s22 op_sel:[0,0,0,1]
	s_add_u32 s24, s0, 0x8000
	ds_write_b128 v142, v[152:155] offset:32768
	ds_write_b128 v143, v[120:123] offset:32768
	s_waitcnt lgkmcnt(0)
	s_barrier
	s_addc_u32 s25, s1, 0
	ds_read_b128 v[64:67], v144 offset:32768
	ds_read_b128 v[68:71], v144 offset:33792
	ds_read_b128 v[72:75], v144 offset:34816
	ds_read_b128 v[76:79], v144 offset:35840
	s_nop 3
	s_waitcnt lgkmcnt(3)
	global_store_dwordx4 v137, v[64:67], s[24:25] sc1
	s_waitcnt lgkmcnt(2)
	global_store_dwordx4 v138, v[68:71], s[24:25] sc1
	s_waitcnt lgkmcnt(1)
	global_store_dwordx4 v139, v[72:75], s[24:25] sc1
	s_waitcnt lgkmcnt(0)
	global_store_dwordx4 v140, v[76:79], s[24:25] sc1
	s_nop 1
	s_add_u32 s0, s0, 0x10000
	s_addc_u32 s1, s1, 0
	s_mov_b64 s[24:25], 0x400000
	s_cmp_lt_u32 s13, 14
	v_lshl_add_u64 v[134:135], v[134:135], 0, s[24:25]
	s_cbranch_scc1 .LBB0_490

; #define G_SCHED __builtin_amdgcn_sched_barrier(0)
; #define CI_LOAD(R, kt) do { _Pragma("unroll") for (int _j = 0; _j < 16; ++_j) R[_j] = __builtin_nontemporal_load((const f32x4*)(src + (size_t)((kt) * 128 + _j) * LDB)); } while (0)
; template <int LDB>
; __device__ __forceinline__ void convert_image(const float* __restrict__ W, int col0, int col1, unsigned char* __restrict__ img, LAS3 char* lds, int wid) {
;     ...
;     f32x4 ra[16], rb[16];
;     CI_LOAD(ra, 0);
;     for (int kt = 0; kt < 16; kt += 2) {
;         CI_LOAD(rb, kt + 1); G_SCHED;
;         CI_CONV(ra, kt); G_SCHED;
;         CI_LOAD(ra, (kt + 2 < 16) ? kt + 2 : 15); G_SCHED;
.Lcw_dn:
	s_waitcnt vmcnt(34)
	v_cvt_scalef32_pk_fp8_f32 v148, v0, v4, s17
	s_waitcnt vmcnt(30)
	v_cvt_scalef32_pk_fp8_f32 v149, v16, v20, s17
	s_waitcnt vmcnt(26)
	v_cvt_scalef32_pk_fp8_f32 v150, v32, v36, s17
	s_waitcnt vmcnt(22)
	v_cvt_scalef32_pk_fp8_f32 v151, v48, v52, s17
	v_cvt_scalef32_pk_fp8_f32 v148, v8, v12, s17 op_sel:[0,0,0,1]
	v_cvt_scalef32_pk_fp8_f32 v149, v24, v28, s17 op_sel:[0,0,0,1]
	v_cvt_scalef32_pk_fp8_f32 v150, v40, v44, s17 op_sel:[0,0,0,1]
	s_waitcnt vmcnt(20)
	v_cvt_scalef32_pk_fp8_f32 v151, v56, v60, s17 op_sel:[0,0,0,1]
	ds_write_b128 v141, v[148:151]
	v_mov_b32_e32 v148, v123
	v_mov_b32_e32 v149, v123
	v_mov_b32_e32 v150, v123
	v_mov_b32_e32 v151, v123
	v_cvt_scalef32_pk_fp8_f32 v148, v1, v5, s17
	v_cvt_scalef32_pk_fp8_f32 v149, v17, v21, s17
	v_cvt_scalef32_pk_fp8_f32 v150, v33, v37, s17
	v_cvt_scalef32_pk_fp8_f32 v151, v49, v53, s17
	v_cvt_scalef32_pk_fp8_f32 v148, v9, v13, s17 op_sel:[0,0,0,1]
	v_cvt_scalef32_pk_fp8_f32 v149, v25, v29, s17 op_sel:[0,0,0,1]
	v_cvt_scalef32_pk_fp8_f32 v150, v41, v45, s17 op_sel:[0,0,0,1]
	v_cvt_scalef32_pk_fp8_f32 v151, v57, v61, s17 op_sel:[0,0,0,1]
	ds_write_b128 v141, v[148:151] offset:128
	v_mov_b32_e32 v148, v123
	v_mov_b32_e32 v0, v123
	v_cvt_scalef32_pk_fp8_f32 v148, v2, v6, s17
	v_mov_b32_e32 v149, v123
	v_mov_b32_e32 v150, v123
	v_mov_b32_e32 v151, v123
	v_cvt_scalef32_pk_fp8_f32 v0, v3, v7, s17
	v_mov_b32_e32 v1, v123
	v_mov_b32_e32 v2, v123
	v_mov_b32_e32 v3, v123
	v_cvt_scalef32_pk_fp8_f32 v149, v18, v22, s17
	v_cvt_scalef32_pk_fp8_f32 v150, v34, v38, s17
	v_cvt_scalef32_pk_fp8_f32 v151, v50, v54, s17
	v_cvt_scalef32_pk_fp8_f32 v1, v19, v23, s17
	v_cvt_scalef32_pk_fp8_f32 v2, v35, v39, s17
	v_cvt_scalef32_pk_fp8_f32 v3, v51, v55, s17
	v_cvt_scalef32_pk_fp8_f32 v148, v10, v14, s17 op_sel:[0,0,0,1]
	v_cvt_scalef32_pk_fp8_f32 v149, v26, v30, s17 op_sel:[0,0,0,1]
	v_cvt_scalef32_pk_fp8_f32 v150, v42, v46, s17 op_sel:[0,0,0,1]
	v_cvt_scalef32_pk_fp8_f32 v151, v58, v62, s17 op_sel:[0,0,0,1]
	v_cvt_scalef32_pk_fp8_f32 v0, v11, v15, s17 op_sel:[0,0,0,1]
	v_cvt_scalef32_pk_fp8_f32 v1, v27, v31, s17 op_sel:[0,0,0,1]
	v_cvt_scalef32_pk_fp8_f32 v2, v43, v47, s17 op_sel:[0,0,0,1]
	v_cvt_scalef32_pk_fp8_f32 v3, v59, v63, s17 op_sel:[0,0,0,1]
	ds_write_b128 v142, v[148:151]
	ds_write_b128 v143, v[0:3]
	s_waitcnt lgkmcnt(0)
	s_barrier
	ds_read_b128 v[0:3], v152
	ds_read_b128 v[4:7], v152 offset:1024
	ds_read_b128 v[8:11], v152 offset:2048
	ds_read_b128 v[12:15], v152 offset:3072
	s_nop 3
	s_waitcnt lgkmcnt(3)
	global_store_dwordx4 v137, v[0:3], s[0:1] sc1
	s_waitcnt lgkmcnt(2)
	global_store_dwordx4 v138, v[4:7], s[0:1] sc1
	s_waitcnt lgkmcnt(1)
	global_store_dwordx4 v139, v[8:11], s[0:1] sc1
	s_waitcnt lgkmcnt(0)
	global_store_dwordx4 v140, v[12:15], s[0:1] sc1
	s_nop 1
	s_cmp_eq_u32 s14, 14
	s_cbranch_scc1 .Lnp_dn
	s_min_u32 s4, s14, 13
	s_lshl_b32 s4, s4, 20
	v_lshl_add_u64 v[56:57], v[132:133], 0, s[4:5]
	s_mov_b32 s4, 0x200000
	v_add_co_u32_e32 v0, vcc, s4, v56
	s_mov_b32 s4, 0x202000
	s_nop 0
	v_addc_co_u32_e32 v1, vcc, 0, v57, vcc
	v_add_co_u32_e32 v4, vcc, s4, v56
	s_mov_b32 s4, 0x204000
	s_nop 0
	v_addc_co_u32_e32 v5, vcc, 0, v57, vcc
	v_add_co_u32_e32 v8, vcc, s4, v56
	s_mov_b32 s4, 0x206000
	s_nop 0
	v_addc_co_u32_e32 v9, vcc, 0, v57, vcc
	v_add_co_u32_e32 v12, vcc, s4, v56
	s_mov_b32 s4, 0x208000
	s_nop 0
	v_addc_co_u32_e32 v13, vcc, 0, v57, vcc
	v_add_co_u32_e32 v16, vcc, s4, v56
	s_mov_b32 s4, 0x20a000
	s_nop 0
	v_addc_co_u32_e32 v17, vcc, 0, v57, vcc
	v_add_co_u32_e32 v20, vcc, s4, v56
	s_mov_b32 s4, 0x20c000
	s_nop 0
	v_addc_co_u32_e32 v21, vcc, 0, v57, vcc
	v_add_co_u32_e32 v24, vcc, s4, v56
	s_mov_b32 s4, 0x20e000
	s_nop 0
	v_addc_co_u32_e32 v25, vcc, 0, v57, vcc
	v_add_co_u32_e32 v28, vcc, s4, v56
	s_mov_b32 s4, 0x210000
	s_nop 0
	v_addc_co_u32_e32 v29, vcc, 0, v57, vcc
	v_add_co_u32_e32 v32, vcc, s4, v56
	s_mov_b32 s4, 0x212000
	s_nop 0
	v_addc_co_u32_e32 v33, vcc, 0, v57, vcc
	v_add_co_u32_e32 v36, vcc, s4, v56
	s_mov_b32 s4, 0x214000
	s_nop 0
	v_addc_co_u32_e32 v37, vcc, 0, v57, vcc
	v_add_co_u32_e32 v40, vcc, s4, v56
	s_mov_b32 s4, 0x216000
	s_nop 0
	v_addc_co_u32_e32 v41, vcc, 0, v57, vcc
	v_add_co_u32_e32 v44, vcc, s4, v56
	s_mov_b32 s4, 0x218000
	s_nop 0
	v_addc_co_u32_e32 v45, vcc, 0, v57, vcc
	v_add_co_u32_e32 v48, vcc, s4, v56
	s_mov_b32 s4, 0x21a000
	s_nop 0
	v_addc_co_u32_e32 v49, vcc, 0, v57, vcc
	v_add_co_u32_e32 v52, vcc, s4, v56
	s_mov_b32 s4, 0x21c000
	s_nop 0
	v_addc_co_u32_e32 v53, vcc, 0, v57, vcc
	v_add_co_u32_e32 v58, vcc, s4, v56
	s_mov_b32 s4, 0x21e000
	s_nop 0
	v_addc_co_u32_e32 v59, vcc, 0, v57, vcc
	v_add_co_u32_e32 v60, vcc, s4, v56
	global_load_dwordx4 v[0:3], v[0:1], off nt
	s_nop 0
	global_load_dwordx4 v[4:7], v[4:5], off nt
	v_addc_co_u32_e32 v61, vcc, 0, v57, vcc
	global_load_dwordx4 v[8:11], v[8:9], off nt
	s_nop 0
	global_load_dwordx4 v[12:15], v[12:13], off nt
	s_nop 0
	global_load_dwordx4 v[16:19], v[16:17], off nt
	s_nop 0
	global_load_dwordx4 v[20:23], v[20:21], off nt
	s_nop 0
	global_load_dwordx4 v[24:27], v[24:25], off nt
	s_nop 0
	global_load_dwordx4 v[28:31], v[28:29], off nt
	s_nop 0
	global_load_dwordx4 v[32:35], v[32:33], off nt
	s_nop 0
	global_load_dwordx4 v[36:39], v[36:37], off nt
	s_nop 0
	global_load_dwordx4 v[40:43], v[40:41], off nt
	s_nop 0
	global_load_dwordx4 v[44:47], v[44:45], off nt
	s_nop 0
	global_load_dwordx4 v[48:51], v[48:49], off nt
	s_nop 0
	global_load_dwordx4 v[52:55], v[52:53], off nt
	s_nop 0
	global_load_dwordx4 v[56:59], v[58:59], off nt
	s_nop 0
	global_load_dwordx4 v[60:63], v[60:61], off nt

; #define G_SCHED __builtin_amdgcn_sched_barrier(0)
; #define CI_LOAD(R, kt) do { _Pragma("unroll") for (int _j = 0; _j < 16; ++_j) R[_j] = __builtin_nontemporal_load((const f32x4*)(src + (size_t)((kt) * 128 + _j) * LDB)); } while (0)
; template <int LDB>
; __device__ __forceinline__ void convert_image(const float* __restrict__ W, int col0, int col1, unsigned char* __restrict__ img, LAS3 char* lds, int wid) {
;     ...
;     f32x4 ra[16], rb[16];
;     CI_LOAD(ra, 0);
;     for (int kt = 0; kt < 16; kt += 2) {
;         CI_LOAD(rb, kt + 1); G_SCHED;
;         CI_CONV(ra, kt); G_SCHED;
;         CI_LOAD(ra, (kt + 2 < 16) ? kt + 2 : 15); G_SCHED;
;         CI_CONV(rb, kt + 1); G_SCHED;
;     }
.Lnw2_dn:
	s_waitcnt vmcnt(20)
	v_cvt_scalef32_pk_fp8_f32 v151, v116, v124, s17 op_sel:[0,0,0,1]
	ds_write_b128 v141, v[148:151] offset:32768
	v_mov_b32_e32 v148, v123
	v_mov_b32_e32 v149, v123
	v_mov_b32_e32 v150, v123
	v_mov_b32_e32 v151, v123
	v_cvt_scalef32_pk_fp8_f32 v148, v129, v65, s17
	v_cvt_scalef32_pk_fp8_f32 v149, v77, v81, s17
	v_cvt_scalef32_pk_fp8_f32 v150, v93, v97, s17
	v_cvt_scalef32_pk_fp8_f32 v151, v109, v113, s17
	v_cvt_scalef32_pk_fp8_f32 v148, v69, v73, s17 op_sel:[0,0,0,1]
	v_cvt_scalef32_pk_fp8_f32 v149, v85, v89, s17 op_sel:[0,0,0,1]
	v_cvt_scalef32_pk_fp8_f32 v150, v101, v105, s17 op_sel:[0,0,0,1]
	v_cvt_scalef32_pk_fp8_f32 v151, v117, v125, s17 op_sel:[0,0,0,1]
	ds_write_b128 v141, v[148:151] offset:32896
	v_mov_b32_e32 v148, v123
	v_mov_b32_e32 v149, v123
	v_mov_b32_e32 v150, v123
	v_mov_b32_e32 v151, v123
	v_mov_b32_e32 v120, v123
	v_mov_b32_e32 v121, v123
	v_mov_b32_e32 v122, v123
	v_cvt_scalef32_pk_fp8_f32 v148, v130, v66, s17
	v_cvt_scalef32_pk_fp8_f32 v149, v78, v82, s17
	v_cvt_scalef32_pk_fp8_f32 v150, v94, v98, s17
	v_cvt_scalef32_pk_fp8_f32 v151, v110, v114, s17
	v_cvt_scalef32_pk_fp8_f32 v120, v131, v67, s17
	v_cvt_scalef32_pk_fp8_f32 v121, v79, v83, s17
	v_cvt_scalef32_pk_fp8_f32 v122, v95, v99, s17
	v_cvt_scalef32_pk_fp8_f32 v123, v111, v115, s17
	v_cvt_scalef32_pk_fp8_f32 v148, v70, v74, s17 op_sel:[0,0,0,1]
	v_cvt_scalef32_pk_fp8_f32 v149, v86, v90, s17 op_sel:[0,0,0,1]
	v_cvt_scalef32_pk_fp8_f32 v150, v102, v106, s17 op_sel:[0,0,0,1]
	v_cvt_scalef32_pk_fp8_f32 v151, v118, v126, s17 op_sel:[0,0,0,1]
	v_cvt_scalef32_pk_fp8_f32 v120, v71, v75, s17 op_sel:[0,0,0,1]
	v_cvt_scalef32_pk_fp8_f32 v121, v87, v91, s17 op_sel:[0,0,0,1]
	v_cvt_scalef32_pk_fp8_f32 v122, v103, v107, s17 op_sel:[0,0,0,1]
	v_cvt_scalef32_pk_fp8_f32 v123, v119, v127, s17 op_sel:[0,0,0,1]
	s_add_u32 s30, s0, 0x8000
	ds_write_b128 v142, v[148:151] offset:32768
	ds_write_b128 v143, v[120:123] offset:32768
	s_waitcnt lgkmcnt(0)
	s_barrier
	s_addc_u32 s31, s1, 0
	ds_read_b128 v[64:67], v152 offset:32768
	ds_read_b128 v[68:71], v152 offset:33792
	ds_read_b128 v[72:75], v152 offset:34816
	ds_read_b128 v[76:79], v152 offset:35840
	s_nop 3
	s_waitcnt lgkmcnt(3)
	global_store_dwordx4 v137, v[64:67], s[30:31] sc1
	s_waitcnt lgkmcnt(2)
	global_store_dwordx4 v138, v[68:71], s[30:31] sc1
	s_waitcnt lgkmcnt(1)
	global_store_dwordx4 v139, v[72:75], s[30:31] sc1
	s_waitcnt lgkmcnt(0)
	global_store_dwordx4 v140, v[76:79], s[30:31] sc1
	s_nop 1
	s_add_u32 s0, s0, 0x10000
	s_addc_u32 s1, s1, 0
	s_mov_b64 s[30:31], 0x200000
	s_cmp_lt_u32 s14, 14
	v_lshl_add_u64 v[134:135], v[134:135], 0, s[30:31]
	s_cbranch_scc1 .LBB0_589
